# P0 weight-conversion and adaLN GEMV loops: counted vmcnt so the next-block prefetch loads stay in flight during convert/store of the current block (hipcc's vmcnt(0) ladders drained them)
# baseline (speedup 1.0000x reference)
; __device__ __forceinline__ f32x4 gld4_nt(const float* p) { return __builtin_nontemporal_load((const GAS f32x4*)p); }
; __device__ __forceinline__ void p0a_mod(const In& I, float* mod, ldsp lds) {
;     ...
;         for (int k0 = 0; k0 < 64; k0 += 8) {
;             if (k0 + 8 < 64) {
; #pragma unroll
;                 for (int j = 0; j < 8; ++j) wn[j] = gld4_nt(w + (size_t)(k0 + 8 + j) * 6144); }
; #pragma unroll
;             for (int j = 0; j < 8; ++j) { a0 += wv[j] * ca[kq * 64 + k0 + j]; a1 += wv[j] * ca[1024 + kq * 64 + k0 + j]; }
; #pragma unroll
;             for (int j = 0; j < 8; ++j) wv[j] = wn[j]; }
.Lp0a_d:
	s_waitcnt vmcnt(0)
	s_branch .LBB0_14
.LBB0_12:
	s_waitcnt vmcnt(0)
	v_mov_b64_e32 v[36:37], v[28:29]
	v_mov_b64_e32 v[34:35], v[26:27]
	v_mov_b32_e32 v46, v2
	v_mov_b32_e32 v47, v3
	v_mov_b32_e32 v48, v4
	v_mov_b32_e32 v49, v5
	v_mov_b32_e32 v42, v6
	v_mov_b32_e32 v43, v7
	v_mov_b32_e32 v44, v8
	v_mov_b32_e32 v45, v9
	v_mov_b32_e32 v50, v10
	v_mov_b32_e32 v51, v11
	v_mov_b32_e32 v52, v12
	v_mov_b32_e32 v53, v13
	v_mov_b32_e32 v38, v14
	v_mov_b32_e32 v39, v15
	v_mov_b32_e32 v40, v16
	v_mov_b32_e32 v41, v17
	v_mov_b32_e32 v58, v18
	v_mov_b32_e32 v59, v19
	v_mov_b32_e32 v60, v20
	v_mov_b32_e32 v61, v21
	v_mov_b32_e32 v54, v22
	v_mov_b32_e32 v55, v23
	v_mov_b32_e32 v56, v24
	v_mov_b32_e32 v57, v25
	v_mov_b32_e32 v62, v30
	v_mov_b32_e32 v63, v31
	v_mov_b32_e32 v64, v32
	v_mov_b32_e32 v65, v33
	s_cmp_gt_u32 s25, 55
	s_cselect_b64 s[8:9], -1, 0
	s_and_b64 vcc, exec, s[8:9]
	s_cbranch_vccnz .LBB0_14

; __device__ __forceinline__ f32x4 gld4_nt(const float* p) { return __builtin_nontemporal_load((const GAS f32x4*)p); }
; __device__ __forceinline__ void p0a_mod(const In& I, float* mod, ldsp lds) {
;     ...
;             if (k0 + 8 < 64) {
; #pragma unroll
;                 for (int j = 0; j < 8; ++j) wn[j] = gld4_nt(w + (size_t)(k0 + 8 + j) * 6144); }
; #pragma unroll
;             for (int j = 0; j < 8; ++j) { a0 += wv[j] * ca[kq * 64 + k0 + j]; a1 += wv[j] * ca[1024 + kq * 64 + k0 + j]; }
; #pragma unroll
;             for (int j = 0; j < 8; ++j) wv[j] = wn[j]; }
;         red[(0 * 16 + kq) * 32 + c4] = a0; red[(1 * 16 + kq) * 32 + c4] = a1;
;         __syncthreads();
;         if (tid < 64) { const int b = tid >> 5; f32x4 s = {0.f, 0.f, 0.f, 0.f};
; #pragma unroll
;             for (int j = 0; j < 16; ++j) s += red[(b * 16 + j) * 32 + c4];
;             gst4(mod + ((size_t)l * 2 + b) * 6144 + n, s + gld4(I.b_ada + (size_t)l * 6144 + n)); }
.LBB0_14:
	ds_read_b128 v[92:95], v91
	ds_read_b128 v[96:99], v91 offset:4096
	ds_read_b128 v[100:103], v91 offset:16
	ds_read_b128 v[104:107], v91 offset:4112
	s_add_i32 s25, s25, 8
	v_lshl_add_u64 v[86:87], v[86:87], 0, s[6:7]
	v_add_u32_e32 v91, 32, v91
	s_waitcnt vmcnt(15) lgkmcnt(3)
	v_pk_fma_f32 v[70:71], v[46:47], v[92:93], v[70:71] op_sel_hi:[1,0,1]
	v_pk_fma_f32 v[72:73], v[48:49], v[92:93], v[72:73] op_sel_hi:[1,0,1]
	s_waitcnt lgkmcnt(2)
	v_pk_fma_f32 v[46:47], v[46:47], v[96:97], v[66:67] op_sel_hi:[1,0,1]
	v_pk_fma_f32 v[48:49], v[48:49], v[96:97], v[68:69] op_sel_hi:[1,0,1]
	s_waitcnt vmcnt(14)
	v_pk_fma_f32 v[66:67], v[44:45], v[92:93], v[72:73] op_sel:[0,1,0]
	v_pk_fma_f32 v[68:69], v[42:43], v[92:93], v[70:71] op_sel:[0,1,0]
	v_pk_fma_f32 v[42:43], v[42:43], v[96:97], v[46:47] op_sel:[0,1,0]
	v_pk_fma_f32 v[44:45], v[44:45], v[96:97], v[48:49] op_sel:[0,1,0]
	s_waitcnt vmcnt(13)
	v_pk_fma_f32 v[46:47], v[50:51], v[94:95], v[68:69] op_sel_hi:[1,0,1]
	v_pk_fma_f32 v[48:49], v[52:53], v[94:95], v[66:67] op_sel_hi:[1,0,1]
	v_pk_fma_f32 v[42:43], v[50:51], v[98:99], v[42:43] op_sel_hi:[1,0,1]
	v_mov_b32_e32 v50, v95
	v_pk_fma_f32 v[44:45], v[52:53], v[98:99], v[44:45] op_sel_hi:[1,0,1]
	s_waitcnt vmcnt(12)
	v_pk_fma_f32 v[48:49], v[40:41], v[50:51], v[48:49] op_sel_hi:[1,0,1]
	v_pk_fma_f32 v[46:47], v[38:39], v[50:51], v[46:47] op_sel_hi:[1,0,1]
	v_mov_b32_e32 v50, v99
	v_pk_fma_f32 v[40:41], v[40:41], v[50:51], v[44:45] op_sel_hi:[1,0,1]
	v_pk_fma_f32 v[38:39], v[38:39], v[50:51], v[42:43] op_sel_hi:[1,0,1]
	s_waitcnt vmcnt(11) lgkmcnt(1)
	v_pk_fma_f32 v[42:43], v[58:59], v[100:101], v[46:47] op_sel_hi:[1,0,1]
	v_pk_fma_f32 v[44:45], v[60:61], v[100:101], v[48:49] op_sel_hi:[1,0,1]
	s_waitcnt lgkmcnt(0)
	v_pk_fma_f32 v[38:39], v[58:59], v[104:105], v[38:39] op_sel_hi:[1,0,1]
	v_pk_fma_f32 v[40:41], v[60:61], v[104:105], v[40:41] op_sel_hi:[1,0,1]
	s_waitcnt vmcnt(10)
	v_pk_fma_f32 v[42:43], v[54:55], v[100:101], v[42:43] op_sel:[0,1,0]
	v_pk_fma_f32 v[44:45], v[56:57], v[100:101], v[44:45] op_sel:[0,1,0]
	v_pk_fma_f32 v[40:41], v[56:57], v[104:105], v[40:41] op_sel:[0,1,0]
	v_pk_fma_f32 v[38:39], v[54:55], v[104:105], v[38:39] op_sel:[0,1,0]
	s_waitcnt vmcnt(9)
	v_pk_fma_f32 v[42:43], v[62:63], v[102:103], v[42:43] op_sel_hi:[1,0,1]
	v_mov_b32_e32 v46, v103
	v_pk_fma_f32 v[44:45], v[64:65], v[102:103], v[44:45] op_sel_hi:[1,0,1]
	v_pk_fma_f32 v[38:39], v[62:63], v[106:107], v[38:39] op_sel_hi:[1,0,1]
	v_pk_fma_f32 v[40:41], v[64:65], v[106:107], v[40:41] op_sel_hi:[1,0,1]
	s_waitcnt vmcnt(8)
	v_pk_fma_f32 v[70:71], v[34:35], v[46:47], v[42:43] op_sel_hi:[1,0,1]
	v_mov_b32_e32 v42, v107
	v_pk_fma_f32 v[72:73], v[36:37], v[46:47], v[44:45] op_sel_hi:[1,0,1]
	v_pk_fma_f32 v[68:69], v[36:37], v[42:43], v[40:41] op_sel_hi:[1,0,1]
	v_pk_fma_f32 v[66:67], v[34:35], v[42:43], v[38:39] op_sel_hi:[1,0,1]
	s_and_b64 vcc, exec, s[8:9]
	s_cbranch_vccz .LBB0_12
	ds_write_b128 v88, v[70:73] offset:8192
	ds_write_b128 v89, v[66:69] offset:16384
	s_waitcnt lgkmcnt(0)
	s_barrier
	s_and_saveexec_b64 s[8:9], s[4:5]
	s_cbranch_execz .LBB0_10
	s_mul_i32 s26, s24, 0x6000
	s_mul_hi_i32 s25, s24, 0x6000
	s_add_u32 s26, s52, s26
	s_addc_u32 s27, s53, s25
	v_lshl_add_u64 v[34:35], s[26:27], 0, v[84:85]
	global_load_dwordx4 v[34:37], v[34:35], off
	ds_read_b128 v[38:41], v76 offset:8192
	ds_read_b128 v[42:45], v76 offset:8704
	ds_read_b128 v[46:49], v76 offset:9216
	ds_read_b128 v[50:53], v76 offset:9728
	ds_read_b128 v[54:57], v76 offset:10240
	ds_read_b128 v[58:61], v76 offset:10752
	ds_read_b128 v[62:65], v76 offset:11264
	ds_read_b128 v[66:69], v76 offset:11776
	ds_read_b128 v[70:73], v76 offset:12288
	ds_read_b128 v[92:95], v76 offset:12800
	ds_read_b128 v[96:99], v76 offset:13312
	ds_read_b128 v[100:103], v76 offset:13824
	ds_read_b128 v[104:107], v76 offset:14336
	ds_read_b128 v[108:111], v76 offset:14848
	ds_read_b128 v[112:115], v76 offset:15360
	ds_read_b128 v[116:119], v76 offset:15872
	s_waitcnt lgkmcnt(14)
	v_pk_add_f32 v[40:41], v[40:41], 0 op_sel_hi:[1,0]
	v_pk_add_f32 v[38:39], v[38:39], 0 op_sel_hi:[1,0]
	v_pk_add_f32 v[40:41], v[40:41], v[44:45]
	v_pk_add_f32 v[38:39], v[38:39], v[42:43]
	s_waitcnt lgkmcnt(13)
	v_pk_add_f32 v[40:41], v[40:41], v[48:49]
	v_pk_add_f32 v[38:39], v[38:39], v[46:47]
	s_waitcnt lgkmcnt(12)
	v_pk_add_f32 v[40:41], v[40:41], v[52:53]
	v_pk_add_f32 v[38:39], v[38:39], v[50:51]
	s_waitcnt lgkmcnt(11)
	v_pk_add_f32 v[40:41], v[40:41], v[56:57]
	v_pk_add_f32 v[38:39], v[38:39], v[54:55]
	s_waitcnt lgkmcnt(10)
	v_pk_add_f32 v[40:41], v[40:41], v[60:61]
	v_pk_add_f32 v[38:39], v[38:39], v[58:59]
	s_waitcnt lgkmcnt(9)
	v_pk_add_f32 v[40:41], v[40:41], v[64:65]
	v_pk_add_f32 v[38:39], v[38:39], v[62:63]
	s_waitcnt lgkmcnt(8)
	v_pk_add_f32 v[40:41], v[40:41], v[68:69]
	v_pk_add_f32 v[38:39], v[38:39], v[66:67]
	s_waitcnt lgkmcnt(7)
	v_pk_add_f32 v[40:41], v[40:41], v[72:73]
	v_pk_add_f32 v[38:39], v[38:39], v[70:71]
	s_waitcnt lgkmcnt(6)
	v_pk_add_f32 v[40:41], v[40:41], v[94:95]
	v_pk_add_f32 v[38:39], v[38:39], v[92:93]
	s_waitcnt lgkmcnt(5)
	v_pk_add_f32 v[40:41], v[40:41], v[98:99]
	v_pk_add_f32 v[38:39], v[38:39], v[96:97]
	s_waitcnt lgkmcnt(4)
	v_pk_add_f32 v[40:41], v[40:41], v[102:103]
	v_pk_add_f32 v[38:39], v[38:39], v[100:101]
	s_waitcnt lgkmcnt(3)
	v_pk_add_f32 v[40:41], v[40:41], v[106:107]
	v_pk_add_f32 v[38:39], v[38:39], v[104:105]
	s_waitcnt lgkmcnt(2)
	v_pk_add_f32 v[40:41], v[40:41], v[110:111]
	v_pk_add_f32 v[38:39], v[38:39], v[108:109]
	v_lshl_or_b32 v91, s24, 1, v74
	v_mov_b64_e32 v[86:87], s[2:3]
	s_waitcnt lgkmcnt(1)
	v_pk_add_f32 v[40:41], v[40:41], v[114:115]
	v_pk_add_f32 v[38:39], v[38:39], v[112:113]
	v_mad_i64_i32 v[86:87], s[24:25], v91, s14, v[86:87]
	s_waitcnt lgkmcnt(0)
	v_pk_add_f32 v[40:41], v[40:41], v[118:119]
	v_pk_add_f32 v[38:39], v[38:39], v[116:117]
	v_lshl_add_u64 v[84:85], v[86:87], 0, v[84:85]
	s_waitcnt vmcnt(0)
	v_pk_add_f32 v[36:37], v[40:41], v[36:37]
	v_pk_add_f32 v[34:35], v[38:39], v[34:35]
	global_store_dwordx4 v[84:85], v[34:37], off
	s_branch .LBB0_10

; #define LAS __attribute__((address_space(3)))
; __device__ __forceinline__ unsigned cvt_pk_bf16(float lo, float hi) { unsigned r; asm volatile("v_cvt_pk_bf16_f32 %0, %1, %2" : "=v"(r) : "v"(lo), "v"(hi)); return r; }
; template <bool OUT8> __device__ __forceinline__ void conv_wide(const float* W0, const float* W1, int srcN, const float* ks0, const float* ks1, int kb_lo, int kb_hi, ...
;     ...
;         for (int c = 0; c < 4; ++c) { LAS unsigned char* tp = tile + (4 * lane + c) * RS;
;             if constexpr (OUT8) { u32x2 w; w.x = cvt4_fp8(v[0][c] * W8_SCALE, v[1][c] * W8_SCALE, v[2][c] * W8_SCALE, v[3][c] * W8_SCALE); w.y = cvt4_fp8(v[4][c] * W8_SCALE, v[5][c] * W8_SCALE, v[6][c] * W8_SCALE, v[7][c] * W8_SCALE);
;                 *(LAS u32x2*)(tp + 8 * wid) = w; }
;             else { u32x2 w0, w1; w0.x = cvt_pk_bf16(v[0][c], v[1][c]); w0.y = cvt_pk_bf16(v[2][c], v[3][c]); w1.x = cvt_pk_bf16(v[4][c], v[5][c]); w1.y = cvt_pk_bf16(v[6][c], v[7][c]);
;                 *(LAS u32x2*)(tp + 16 * wid) = w0; *(LAS u32x2*)(tp + 16 * wid + 8) = w1; } }
;         __syncthreads();
;         { const int row = tid >> 1, hf = tid & 1;
;           if constexpr (OUT8) { const LAS unsigned char* tp = tile + row * RS + hf * 32; unsigned char* dp = dst + (size_t)(n0 + row) * ldk + kb * 64 + hf * 32;
; #pragma unroll
;               for (int q = 0; q < 2; ++q) { const u32x2 lo = *(const LAS u32x2*)(tp + q * 16), hi2 = *(const LAS u32x2*)(tp + q * 16 + 8); gst16(dp + q * 16, (u32x4){lo.x, lo.y, hi2.x, hi2.y}); } }
;           else { const LAS unsigned char* tp = tile + row * RS + hf * 64; bf16_t* dp = (bf16_t*)dst + (size_t)(n0 + row) * ldk + kb * 64 + hf * 32;
; #pragma unroll
;               for (int q = 0; q < 4; ++q) { const u32x2 lo = *(const LAS u32x2*)(tp + q * 16), hi2 = *(const LAS u32x2*)(tp + q * 16 + 8); gst16(dp + q * 8, (u32x4){lo.x, lo.y, hi2.x, hi2.y}); } } }
;         __syncthreads();
; #pragma unroll
;         for (int j = 0; j < 8; ++j) v[j] = vn[j];
.LBB0_101:
	s_waitcnt vmcnt(14)
	v_cvt_pk_bf16_f32 v74, v20, v32
	v_add_u32_e32 v20, s46, v79
	s_waitcnt vmcnt(12)
	v_cvt_pk_bf16_f32 v75, v44, v48
	s_waitcnt vmcnt(10)
	v_cvt_pk_bf16_f32 v76, v52, v56
	s_waitcnt vmcnt(8)
	v_cvt_pk_bf16_f32 v77, v60, v64
	ds_write_b128 v20, v[74:77]
	v_cvt_pk_bf16_f32 v32, v21, v33
	v_cvt_pk_bf16_f32 v33, v45, v49
	v_cvt_pk_bf16_f32 v44, v53, v57
	v_cvt_pk_bf16_f32 v45, v61, v65
	ds_write2_b64 v20, v[32:33], v[44:45] offset0:17 offset1:18
	v_cvt_pk_bf16_f32 v74, v22, v34
	v_cvt_pk_bf16_f32 v75, v46, v50
	v_cvt_pk_bf16_f32 v76, v54, v58
	v_cvt_pk_bf16_f32 v77, v62, v66
	ds_write_b128 v20, v[74:77] offset:272
	v_cvt_pk_bf16_f32 v22, v23, v35
	v_cvt_pk_bf16_f32 v23, v47, v51
	v_cvt_pk_bf16_f32 v32, v55, v59
	v_cvt_pk_bf16_f32 v33, v63, v67
	v_add_u32_e32 v21, v1, v88
	ds_write2_b64 v20, v[22:23], v[32:33] offset0:51 offset1:52
	s_waitcnt lgkmcnt(0)
	s_barrier
	ds_read2_b64 v[32:35], v21 offset1:1
	ds_read2_b64 v[44:47], v21 offset0:2 offset1:3
	ds_read2_b64 v[48:51], v21 offset0:4 offset1:5
	ds_read2_b64 v[52:55], v21 offset0:6 offset1:7
	s_add_u32 s42, s42, 0x40000
	s_addc_u32 s43, s43, 0
	s_waitcnt lgkmcnt(3)
	global_store_dwordx4 v[72:73], v[32:35], off offset:-32
	s_waitcnt lgkmcnt(2)
	global_store_dwordx4 v[72:73], v[44:47], off offset:-16
	s_waitcnt lgkmcnt(1)
	global_store_dwordx4 v[72:73], v[48:51], off
	s_waitcnt lgkmcnt(0)
	global_store_dwordx4 v[72:73], v[52:55], off offset:16
	s_cmp_eq_u32 s42, 0x1c0000
	v_lshl_add_u64 v[72:73], v[72:73], 0, s[34:35]
	s_barrier
	s_waitcnt vmcnt(4)
	s_cbranch_scc0 .LBB0_99
	s_add_u32 s42, s56, s33
	s_addc_u32 s43, s57, 0
	v_lshl_add_u64 v[22:23], v[2:3], 1, s[42:43]
	v_lshlrev_b32_e32 v2, 1, v90
	v_cvt_pk_bf16_f32 v32, v4, v8
	v_cvt_pk_bf16_f32 v33, v12, v16
	v_cvt_pk_bf16_f32 v34, v24, v28
	v_cvt_pk_bf16_f32 v35, v36, v40
	ds_write_b128 v20, v[32:35]
	v_cvt_pk_bf16_f32 v4, v5, v9
	v_cvt_pk_bf16_f32 v5, v13, v17
	v_lshl_add_u64 v[44:45], v[22:23], 0, v[2:3]
	v_cvt_pk_bf16_f32 v8, v25, v29
	v_cvt_pk_bf16_f32 v9, v37, v41
	ds_write2_b64 v20, v[4:5], v[8:9] offset0:17 offset1:18
	v_cvt_pk_bf16_f32 v22, v6, v10
	v_cvt_pk_bf16_f32 v23, v14, v18
	v_cvt_pk_bf16_f32 v24, v26, v30
	v_cvt_pk_bf16_f32 v25, v38, v42
	ds_write_b128 v20, v[22:25] offset:272
	v_cvt_pk_bf16_f32 v4, v7, v11
	v_cvt_pk_bf16_f32 v5, v15, v19
	v_cvt_pk_bf16_f32 v6, v27, v31
	v_cvt_pk_bf16_f32 v7, v39, v43
	ds_write2_b64 v20, v[4:5], v[6:7] offset0:51 offset1:52
	s_waitcnt lgkmcnt(0)
	s_barrier
	ds_read2_b64 v[4:7], v21 offset1:1
	ds_read2_b64 v[8:11], v21 offset0:2 offset1:3
	ds_read2_b64 v[12:15], v21 offset0:4 offset1:5
	ds_read2_b64 v[16:19], v21 offset0:6 offset1:7
	s_addk_i32 s30, 0x380
	v_lshl_add_u64 v[20:21], v[44:45], 0, s[30:31]
	s_waitcnt lgkmcnt(3)
	global_store_dwordx4 v[20:21], v[4:7], off
	s_waitcnt lgkmcnt(2)
	global_store_dwordx4 v[20:21], v[8:11], off offset:16
	s_waitcnt lgkmcnt(1)
	global_store_dwordx4 v[20:21], v[12:15], off offset:32
	s_waitcnt lgkmcnt(0)
	global_store_dwordx4 v[20:21], v[16:19], off offset:48
	s_barrier
	s_mov_b64 s[42:43], -1
	s_and_b64 vcc, exec, s[0:1]
	s_cbranch_vccz .LBB0_110
	s_branch .LBB0_105

; #define LAS __attribute__((address_space(3)))
; __device__ __forceinline__ unsigned cvt_pk_bf16(float lo, float hi) { unsigned r; asm volatile("v_cvt_pk_bf16_f32 %0, %1, %2" : "=v"(r) : "v"(lo), "v"(hi)); return r; }
; template <bool OUT8> __device__ __forceinline__ void conv_wide(const float* W0, const float* W1, int srcN, const float* ks0, const float* ks1, int kb_lo, int kb_hi, ...
;     ...
;         if (shl) {
; #pragma unroll
;             for (int j = 0; j < 8; ++j) { b0 += v[j] * shl[k0 + j]; b1 += v[j] * shl[1024 + k0 + j]; } }
; #pragma unroll
;         for (int c = 0; c < 4; ++c) { LAS unsigned char* tp = tile + (4 * lane + c) * RS;
;             if constexpr (OUT8) { u32x2 w; w.x = cvt4_fp8(v[0][c] * W8_SCALE, v[1][c] * W8_SCALE, v[2][c] * W8_SCALE, v[3][c] * W8_SCALE); w.y = cvt4_fp8(v[4][c] * W8_SCALE, v[5][c] * W8_SCALE, v[6][c] * W8_SCALE, v[7][c] * W8_SCALE);
;                 *(LAS u32x2*)(tp + 8 * wid) = w; }
;             else { u32x2 w0, w1; w0.x = cvt_pk_bf16(v[0][c], v[1][c]); w0.y = cvt_pk_bf16(v[2][c], v[3][c]); w1.x = cvt_pk_bf16(v[4][c], v[5][c]); w1.y = cvt_pk_bf16(v[6][c], v[7][c]);
;                 *(LAS u32x2*)(tp + 16 * wid) = w0; *(LAS u32x2*)(tp + 16 * wid + 8) = w1; } }
;         __syncthreads();
;         { const int row = tid >> 1, hf = tid & 1;
;           if constexpr (OUT8) { const LAS unsigned char* tp = tile + row * RS + hf * 32; unsigned char* dp = dst + (size_t)(n0 + row) * ldk + kb * 64 + hf * 32;
; #pragma unroll
;               for (int q = 0; q < 2; ++q) { const u32x2 lo = *(const LAS u32x2*)(tp + q * 16), hi2 = *(const LAS u32x2*)(tp + q * 16 + 8); gst16(dp + q * 16, (u32x4){lo.x, lo.y, hi2.x, hi2.y}); } }
;           else { const LAS unsigned char* tp = tile + row * RS + hf * 64; bf16_t* dp = (bf16_t*)dst + (size_t)(n0 + row) * ldk + kb * 64 + hf * 32;
; #pragma unroll
;               for (int q = 0; q < 4; ++q) { const u32x2 lo = *(const LAS u32x2*)(tp + q * 16), hi2 = *(const LAS u32x2*)(tp + q * 16 + 8); gst16(dp + q * 8, (u32x4){lo.x, lo.y, hi2.x, hi2.y}); } } }
;         __syncthreads();
; #pragma unroll
;         for (int j = 0; j < 8; ++j) v[j] = vn[j];
.LBB0_108:
	s_add_i32 s77, s76, s45
	s_add_i32 s78, s77, 0x12800
	s_add_i32 s79, s77, 0x13800
	v_mov_b32_e32 v137, s78
	ds_read_b128 v[138:141], v137
	v_mov_b32_e32 v137, s79
	ds_read_b128 v[142:145], v137
	s_add_i32 s78, s77, 0x12810
	s_add_i32 s77, s77, 0x13810
	s_waitcnt lgkmcnt(1)
	v_pk_fma_f32 v[72:73], v[40:41], v[138:139], v[72:73] op_sel_hi:[1,0,1]
	v_pk_fma_f32 v[76:77], v[42:43], v[138:139], v[76:77] op_sel_hi:[1,0,1]
	s_waitcnt lgkmcnt(0)
	v_pk_fma_f32 v[70:71], v[42:43], v[142:143], v[70:71] op_sel_hi:[1,0,1]
	v_pk_fma_f32 v[124:125], v[40:41], v[142:143], v[124:125] op_sel_hi:[1,0,1]
	v_pk_fma_f32 v[76:77], v[46:47], v[138:139], v[76:77] op_sel:[0,1,0]
	v_pk_fma_f32 v[72:73], v[44:45], v[138:139], v[72:73] op_sel:[0,1,0]
	v_pk_fma_f32 v[70:71], v[46:47], v[142:143], v[70:71] op_sel:[0,1,0]
	v_pk_fma_f32 v[124:125], v[44:45], v[142:143], v[124:125] op_sel:[0,1,0]
	v_pk_fma_f32 v[72:73], v[48:49], v[140:141], v[72:73] op_sel_hi:[1,0,1]
	v_pk_fma_f32 v[76:77], v[50:51], v[140:141], v[76:77] op_sel_hi:[1,0,1]
	v_pk_fma_f32 v[142:143], v[50:51], v[144:145], v[70:71] op_sel_hi:[1,0,1]
	v_mov_b32_e32 v70, v141
	v_pk_fma_f32 v[76:77], v[54:55], v[70:71], v[76:77] op_sel_hi:[1,0,1]
	v_pk_fma_f32 v[146:147], v[52:53], v[70:71], v[72:73] op_sel_hi:[1,0,1]
	v_mov_b32_e32 v70, s78
	v_mov_b32_e32 v137, s77
	ds_read_b128 v[70:73], v70
	ds_read_b128 v[138:141], v137
	v_pk_fma_f32 v[124:125], v[48:49], v[144:145], v[124:125] op_sel_hi:[1,0,1]
	v_mov_b32_e32 v144, v145
	v_pk_fma_f32 v[142:143], v[54:55], v[144:145], v[142:143] op_sel_hi:[1,0,1]
	v_pk_fma_f32 v[124:125], v[52:53], v[144:145], v[124:125] op_sel_hi:[1,0,1]
	s_waitcnt vmcnt(9) lgkmcnt(1)
	v_pk_fma_f32 v[144:145], v[56:57], v[70:71], v[146:147] op_sel_hi:[1,0,1]
	v_pk_fma_f32 v[76:77], v[58:59], v[70:71], v[76:77] op_sel_hi:[1,0,1]
	s_waitcnt lgkmcnt(0)
	v_pk_fma_f32 v[142:143], v[58:59], v[138:139], v[142:143] op_sel_hi:[1,0,1]
	v_pk_fma_f32 v[124:125], v[56:57], v[138:139], v[124:125] op_sel_hi:[1,0,1]
	s_waitcnt vmcnt(8)
	v_pk_fma_f32 v[76:77], v[66:67], v[70:71], v[76:77] op_sel:[0,1,0]
	v_pk_fma_f32 v[70:71], v[64:65], v[70:71], v[144:145] op_sel:[0,1,0]
	v_pk_fma_f32 v[142:143], v[66:67], v[138:139], v[142:143] op_sel:[0,1,0]
	v_pk_fma_f32 v[124:125], v[64:65], v[138:139], v[124:125] op_sel:[0,1,0]
	v_pk_fma_f32 v[70:71], v[60:61], v[72:73], v[70:71] op_sel_hi:[1,0,1]
	v_pk_fma_f32 v[76:77], v[62:63], v[72:73], v[76:77] op_sel_hi:[1,0,1]
	v_pk_fma_f32 v[138:139], v[62:63], v[140:141], v[142:143] op_sel_hi:[1,0,1]
	v_mov_b32_e32 v72, v73
	v_mov_b32_e32 v142, v141
	v_pk_fma_f32 v[76:77], v[38:39], v[72:73], v[76:77] op_sel_hi:[1,0,1]
	v_pk_fma_f32 v[72:73], v[36:37], v[72:73], v[70:71] op_sel_hi:[1,0,1]
	v_pk_fma_f32 v[70:71], v[38:39], v[142:143], v[138:139] op_sel_hi:[1,0,1]
	v_add_u32_e32 v38, s75, v79
	v_pk_fma_f32 v[124:125], v[60:61], v[140:141], v[124:125] op_sel_hi:[1,0,1]
	v_cvt_pk_bf16_f32 v138, v40, v44
	v_cvt_pk_bf16_f32 v139, v48, v52
	v_cvt_pk_bf16_f32 v140, v56, v64
	v_cvt_pk_bf16_f32 v141, v60, v129
	ds_write_b128 v38, v[138:141]
	v_cvt_pk_bf16_f32 v40, v41, v45
	v_cvt_pk_bf16_f32 v41, v49, v53
	v_cvt_pk_bf16_f32 v44, v57, v65
	v_cvt_pk_bf16_f32 v45, v61, v128
	ds_write2_b64 v38, v[40:41], v[44:45] offset0:17 offset1:18
	v_cvt_pk_bf16_f32 v138, v42, v46
	v_cvt_pk_bf16_f32 v139, v50, v54
	v_cvt_pk_bf16_f32 v140, v58, v66
	v_cvt_pk_bf16_f32 v141, v62, v127
	ds_write_b128 v38, v[138:141] offset:272
	v_cvt_pk_bf16_f32 v40, v43, v47
	v_cvt_pk_bf16_f32 v41, v51, v55
	v_cvt_pk_bf16_f32 v42, v59, v67
	v_cvt_pk_bf16_f32 v43, v63, v126
	v_add_u32_e32 v39, v1, v88
	ds_write2_b64 v38, v[40:41], v[42:43] offset0:51 offset1:52
	s_waitcnt lgkmcnt(0)
	s_barrier
	ds_read2_b64 v[40:43], v39 offset1:1
	ds_read2_b64 v[44:47], v39 offset0:2 offset1:3
	ds_read2_b64 v[48:51], v39 offset0:4 offset1:5
	ds_read2_b64 v[52:55], v39 offset0:6 offset1:7
	s_addk_i32 s45, 0x100
	s_mov_b64 s[78:79], 0xa0000
	v_pk_fma_f32 v[124:125], v[36:37], v[142:143], v[124:125] op_sel_hi:[1,0,1]
	s_waitcnt lgkmcnt(3)
	global_store_dwordx4 v[74:75], v[40:43], off offset:-32
	s_waitcnt lgkmcnt(2)
	global_store_dwordx4 v[74:75], v[44:47], off offset:-16
	s_waitcnt lgkmcnt(1)
	global_store_dwordx4 v[74:75], v[48:51], off
	s_waitcnt lgkmcnt(0)
	global_store_dwordx4 v[74:75], v[52:55], off offset:16
	v_lshl_add_u64 v[68:69], v[68:69], 0, s[78:79]
	s_cmpk_lg_i32 s45, 0x700
	v_lshl_add_u64 v[74:75], v[74:75], 0, s[34:35]
	s_barrier
	s_waitcnt vmcnt(4)
	s_cbranch_scc1 .LBB0_106
; template <bool OUT8> __device__ __forceinline__ void conv_wide(const float* W0, const float* W1, int srcN, const float* ks0, const float* ks1, int kb_lo, int kb_hi, ...
;     ...
;         if (shl) {
; #pragma unroll
;             for (int j = 0; j < 8; ++j) { b0 += v[j] * shl[k0 + j]; b1 += v[j] * shl[1024 + k0 + j]; } }
; #pragma unroll
;         for (int c = 0; c < 4; ++c) { LAS unsigned char* tp = tile + (4 * lane + c) * RS;
;             if constexpr (OUT8) { u32x2 w; w.x = cvt4_fp8(v[0][c] * W8_SCALE, v[1][c] * W8_SCALE, v[2][c] * W8_SCALE, v[3][c] * W8_SCALE); w.y = cvt4_fp8(v[4][c] * W8_SCALE, v[5][c] * W8_SCALE, v[6][c] * W8_SCALE, v[7][c] * W8_SCALE);
;                 *(LAS u32x2*)(tp + 8 * wid) = w; }
;             else { u32x2 w0, w1; w0.x = cvt_pk_bf16(v[0][c], v[1][c]); w0.y = cvt_pk_bf16(v[2][c], v[3][c]); w1.x = cvt_pk_bf16(v[4][c], v[5][c]); w1.y = cvt_pk_bf16(v[6][c], v[7][c]);
;                 *(LAS u32x2*)(tp + 16 * wid) = w0; *(LAS u32x2*)(tp + 16 * wid + 8) = w1; } }
;         __syncthreads();
;         { const int row = tid >> 1, hf = tid & 1;
;           if constexpr (OUT8) { const LAS unsigned char* tp = tile + row * RS + hf * 32; unsigned char* dp = dst + (size_t)(n0 + row) * ldk + kb * 64 + hf * 32;
; #pragma unroll
;               for (int q = 0; q < 2; ++q) { const u32x2 lo = *(const LAS u32x2*)(tp + q * 16), hi2 = *(const LAS u32x2*)(tp + q * 16 + 8); gst16(dp + q * 16, (u32x4){lo.x, lo.y, hi2.x, hi2.y}); } }
;           else { const LAS unsigned char* tp = tile + row * RS + hf * 64; bf16_t* dp = (bf16_t*)dst + (size_t)(n0 + row) * ldk + kb * 64 + hf * 32;
; #pragma unroll
;               for (int q = 0; q < 4; ++q) { const u32x2 lo = *(const LAS u32x2*)(tp + q * 16), hi2 = *(const LAS u32x2*)(tp + q * 16 + 8); gst16(dp + q * 8, (u32x4){lo.x, lo.y, hi2.x, hi2.y}); } } }
;         __syncthreads();
; #pragma unroll
;         for (int j = 0; j < 8; ++j) v[j] = vn[j];
;     }
;     if (shl) {
; #pragma unroll
;         for (int c = 0; c < 4; ++c) { red[(0 * 8 + wid) * 256 + 4 * lane + c] = b0[c]; red[(1 * 8 + wid) * 256 + 4 * lane + c] = b1[c]; }
;         __syncthreads();
;         { const int b = tid >> 8, n = tid & 255; float a = 0.f;
; #pragma unroll
;           for (int j = 0; j < 8; ++j) a += red[(b * 8 + j) * 256 + n];
;           atomicAdd((b ? bias1 : bias0) + n0 + n, a); }
;         __syncthreads();
	s_add_u32 s44, s64, s73
	s_addc_u32 s45, s65, 0
	s_add_i32 s47, s30, 7
	s_add_i32 s46, s55, 0
	s_lshl_b32 s30, s47, 8
	s_add_i32 s46, s46, s30
	s_and_b64 s[42:43], s[42:43], exec
	s_cselect_b32 s30, 0xa000, 0
	s_lshl_b32 s33, s33, 2
	s_add_i32 s33, s46, s33
	s_add_i32 s33, s33, 0x10800
	v_mov_b32_e32 v52, s33
	ds_read_b128 v[40:43], v52 offset:8192
	ds_read_b128 v[44:47], v52 offset:12288
	ds_read_b128 v[48:51], v52 offset:8208
	v_lshl_add_u64 v[36:37], v[2:3], 1, s[44:45]
	v_lshlrev_b32_e32 v2, 1, v90
	v_lshl_add_u64 v[36:37], v[36:37], 0, v[2:3]
	s_waitcnt lgkmcnt(2)
	v_pk_fma_f32 v[56:57], v[4:5], v[40:41], v[72:73] op_sel_hi:[1,0,1]
	v_pk_fma_f32 v[58:59], v[6:7], v[40:41], v[76:77] op_sel_hi:[1,0,1]
	v_mov_b32_e32 v2, v43
	v_pk_fma_f32 v[58:59], v[10:11], v[40:41], v[58:59] op_sel:[0,1,0]
	v_pk_fma_f32 v[40:41], v[8:9], v[40:41], v[56:57] op_sel:[0,1,0]
	v_pk_fma_f32 v[58:59], v[14:15], v[42:43], v[58:59] op_sel_hi:[1,0,1]
	v_pk_fma_f32 v[40:41], v[12:13], v[42:43], v[40:41] op_sel_hi:[1,0,1]
	s_waitcnt lgkmcnt(1)
	v_pk_fma_f32 v[60:61], v[4:5], v[44:45], v[124:125] op_sel_hi:[1,0,1]
	v_pk_fma_f32 v[62:63], v[6:7], v[44:45], v[70:71] op_sel_hi:[1,0,1]
	v_pk_fma_f32 v[42:43], v[18:19], v[2:3], v[58:59] op_sel_hi:[1,0,1]
	v_pk_fma_f32 v[40:41], v[16:17], v[2:3], v[40:41] op_sel_hi:[1,0,1]
	ds_read_b128 v[52:55], v52 offset:12304
	v_pk_fma_f32 v[56:57], v[10:11], v[44:45], v[62:63] op_sel:[0,1,0]
	v_pk_fma_f32 v[44:45], v[8:9], v[44:45], v[60:61] op_sel:[0,1,0]
	s_waitcnt lgkmcnt(1)
	v_pk_fma_f32 v[40:41], v[20:21], v[48:49], v[40:41] op_sel_hi:[1,0,1]
	v_pk_fma_f32 v[42:43], v[22:23], v[48:49], v[42:43] op_sel_hi:[1,0,1]
	v_pk_fma_f32 v[44:45], v[12:13], v[46:47], v[44:45] op_sel_hi:[1,0,1]
	v_pk_fma_f32 v[56:57], v[14:15], v[46:47], v[56:57] op_sel_hi:[1,0,1]
	v_mov_b32_e32 v2, v47
	v_pk_fma_f32 v[42:43], v[26:27], v[48:49], v[42:43] op_sel:[0,1,0]
	v_pk_fma_f32 v[40:41], v[24:25], v[48:49], v[40:41] op_sel:[0,1,0]
	v_pk_fma_f32 v[46:47], v[18:19], v[2:3], v[56:57] op_sel_hi:[1,0,1]
	v_pk_fma_f32 v[44:45], v[16:17], v[2:3], v[44:45] op_sel_hi:[1,0,1]
	v_pk_fma_f32 v[40:41], v[28:29], v[50:51], v[40:41] op_sel_hi:[1,0,1]
	v_pk_fma_f32 v[42:43], v[30:31], v[50:51], v[42:43] op_sel_hi:[1,0,1]
	v_mov_b32_e32 v2, v51
	v_cvt_pk_bf16_f32 v48, v4, v8
	v_cvt_pk_bf16_f32 v49, v12, v16
	v_cvt_pk_bf16_f32 v50, v20, v24
	v_cvt_pk_bf16_f32 v51, v28, v32
	ds_write_b128 v38, v[48:51]
	v_cvt_pk_bf16_f32 v4, v5, v9
	v_cvt_pk_bf16_f32 v5, v13, v17
	v_cvt_pk_bf16_f32 v8, v21, v25
	v_cvt_pk_bf16_f32 v9, v29, v33
	ds_write2_b64 v38, v[4:5], v[8:9] offset0:17 offset1:18
	v_cvt_pk_bf16_f32 v48, v6, v10
	v_cvt_pk_bf16_f32 v49, v14, v18
	v_cvt_pk_bf16_f32 v50, v22, v26
	v_cvt_pk_bf16_f32 v51, v30, v34
	ds_write_b128 v38, v[48:51] offset:272
	v_cvt_pk_bf16_f32 v4, v7, v11
	v_cvt_pk_bf16_f32 v5, v15, v19
	v_cvt_pk_bf16_f32 v6, v23, v27
	v_cvt_pk_bf16_f32 v7, v31, v35
	ds_write2_b64 v38, v[4:5], v[6:7] offset0:51 offset1:52
	s_waitcnt lgkmcnt(0)
	s_barrier
	ds_read2_b64 v[4:7], v39 offset1:1
	ds_read2_b64 v[8:11], v39 offset0:2 offset1:3
	ds_read2_b64 v[12:15], v39 offset0:4 offset1:5
	ds_read2_b64 v[16:19], v39 offset0:6 offset1:7
	v_pk_fma_f32 v[44:45], v[20:21], v[52:53], v[44:45] op_sel_hi:[1,0,1]
	v_pk_fma_f32 v[46:47], v[22:23], v[52:53], v[46:47] op_sel_hi:[1,0,1]
	v_pk_fma_f32 v[44:45], v[24:25], v[52:53], v[44:45] op_sel:[0,1,0]
	v_pk_fma_f32 v[46:47], v[26:27], v[52:53], v[46:47] op_sel:[0,1,0]
	v_pk_fma_f32 v[44:45], v[28:29], v[54:55], v[44:45] op_sel_hi:[1,0,1]
	v_pk_fma_f32 v[46:47], v[30:31], v[54:55], v[46:47] op_sel_hi:[1,0,1]
	v_pk_fma_f32 v[42:43], v[34:35], v[2:3], v[42:43] op_sel_hi:[1,0,1]
	v_pk_fma_f32 v[40:41], v[32:33], v[2:3], v[40:41] op_sel_hi:[1,0,1]
	v_mov_b32_e32 v2, v55
	s_lshl_b32 s42, s47, 7
	s_mov_b32 s43, s31
	v_pk_fma_f32 v[46:47], v[34:35], v[2:3], v[46:47] op_sel_hi:[1,0,1]
	v_pk_fma_f32 v[44:45], v[32:33], v[2:3], v[44:45] op_sel_hi:[1,0,1]
	v_lshl_add_u64 v[20:21], v[36:37], 0, s[42:43]
	v_lshl_add_u32 v2, s1, 10, v133
	s_waitcnt lgkmcnt(3)
	global_store_dwordx4 v[20:21], v[4:7], off
	s_waitcnt lgkmcnt(2)
	global_store_dwordx4 v[20:21], v[8:11], off offset:16
	s_waitcnt lgkmcnt(1)
	global_store_dwordx4 v[20:21], v[12:15], off offset:32
	s_waitcnt lgkmcnt(0)
	global_store_dwordx4 v[20:21], v[16:19], off offset:48
	s_barrier
	ds_write_b128 v2, v[40:43] offset:34816
	ds_write_b128 v2, v[44:47] offset:43008
	v_add_u32_e32 v2, v81, v83
	s_waitcnt lgkmcnt(0)
	s_barrier
	ds_read2st64_b32 v[4:5], v2 offset0:136 offset1:140
	ds_read2st64_b32 v[6:7], v2 offset0:144 offset1:148
	ds_read2st64_b32 v[8:9], v2 offset0:152 offset1:156
	s_mov_b32 s1, s31
	s_mov_b64 s[42:43], -1
	s_waitcnt lgkmcnt(2)
	v_add_f32_e32 v4, 0, v4
	v_add_f32_e32 v10, v4, v5
	ds_read2st64_b32 v[4:5], v2 offset0:160 offset1:164
	s_waitcnt lgkmcnt(2)
	v_add_f32_e32 v2, v10, v6
	v_add_f32_e32 v2, v2, v7
	s_waitcnt lgkmcnt(1)
	v_add_f32_e32 v2, v2, v8
	v_add_f32_e32 v2, v2, v9
	s_waitcnt lgkmcnt(0)
	v_add_f32_e32 v2, v2, v4
	v_add_f32_e32 v6, v2, v5
	v_lshl_add_u64 v[4:5], v[84:85], 0, s[30:31]
	v_lshl_add_u64 v[4:5], s[0:1], 2, v[4:5]
	v_lshlrev_b32_e32 v2, 2, v98
	v_lshl_add_u64 v[4:5], v[4:5], 0, v[2:3]
	global_atomic_add_f32 v[4:5], v6, off
	s_barrier

; #define LAS __attribute__((address_space(3)))
; __device__ __forceinline__ unsigned cvt_pk_bf16(float lo, float hi) { unsigned r; asm volatile("v_cvt_pk_bf16_f32 %0, %1, %2" : "=v"(r) : "v"(lo), "v"(hi)); return r; }
; template <bool OUT8> __device__ __forceinline__ void conv_wide(const float* W0, const float* W1, int srcN, const float* ks0, const float* ks1, int kb_lo, int kb_hi, ...
;     ...
;         for (int c = 0; c < 4; ++c) { LAS unsigned char* tp = tile + (4 * lane + c) * RS;
;             if constexpr (OUT8) { u32x2 w; w.x = cvt4_fp8(v[0][c] * W8_SCALE, v[1][c] * W8_SCALE, v[2][c] * W8_SCALE, v[3][c] * W8_SCALE); w.y = cvt4_fp8(v[4][c] * W8_SCALE, v[5][c] * W8_SCALE, v[6][c] * W8_SCALE, v[7][c] * W8_SCALE);
;                 *(LAS u32x2*)(tp + 8 * wid) = w; }
;             else { u32x2 w0, w1; w0.x = cvt_pk_bf16(v[0][c], v[1][c]); w0.y = cvt_pk_bf16(v[2][c], v[3][c]); w1.x = cvt_pk_bf16(v[4][c], v[5][c]); w1.y = cvt_pk_bf16(v[6][c], v[7][c]);
;                 *(LAS u32x2*)(tp + 16 * wid) = w0; *(LAS u32x2*)(tp + 16 * wid + 8) = w1; } }
;         __syncthreads();
;         { const int row = tid >> 1, hf = tid & 1;
;           if constexpr (OUT8) { const LAS unsigned char* tp = tile + row * RS + hf * 32; unsigned char* dp = dst + (size_t)(n0 + row) * ldk + kb * 64 + hf * 32;
; #pragma unroll
;               for (int q = 0; q < 2; ++q) { const u32x2 lo = *(const LAS u32x2*)(tp + q * 16), hi2 = *(const LAS u32x2*)(tp + q * 16 + 8); gst16(dp + q * 16, (u32x4){lo.x, lo.y, hi2.x, hi2.y}); } }
;           else { const LAS unsigned char* tp = tile + row * RS + hf * 64; bf16_t* dp = (bf16_t*)dst + (size_t)(n0 + row) * ldk + kb * 64 + hf * 32;
; #pragma unroll
;               for (int q = 0; q < 4; ++q) { const u32x2 lo = *(const LAS u32x2*)(tp + q * 16), hi2 = *(const LAS u32x2*)(tp + q * 16 + 8); gst16(dp + q * 8, (u32x4){lo.x, lo.y, hi2.x, hi2.y}); } } }
;         __syncthreads();
; #pragma unroll
;         for (int j = 0; j < 8; ++j) v[j] = vn[j];
.LBB0_112:
	s_waitcnt vmcnt(15)
	v_mul_f32_e32 v2, 0x42800000, v4
	s_waitcnt vmcnt(14)
	v_mul_f32_e32 v4, 0x42800000, v8
	v_med3_f32 v2, v2, s72, v91
	v_med3_f32 v4, v4, s72, v91
	v_mov_b32_e32 v74, 0
	v_cvt_pk_fp8_f32 v74, v2, v4
	s_waitcnt vmcnt(13)
	v_mul_f32_e32 v8, 0x42800000, v16
	s_waitcnt vmcnt(12)
	v_mul_f32_e32 v2, 0x42800000, v12
	v_med3_f32 v4, v8, s72, v91
	v_med3_f32 v2, v2, s72, v91
	v_cvt_pk_fp8_f32 v74, v4, v2 op_sel:[0,0,1]
	s_waitcnt vmcnt(11)
	v_mul_f32_e32 v2, 0x42800000, v20
	s_waitcnt vmcnt(10)
	v_mul_f32_e32 v4, 0x42800000, v24
	v_med3_f32 v2, v2, s72, v91
	v_med3_f32 v4, v4, s72, v91
	v_mov_b32_e32 v75, 0
	v_cvt_pk_fp8_f32 v75, v2, v4
	s_waitcnt vmcnt(9)
	v_mul_f32_e32 v8, 0x42800000, v40
	s_waitcnt vmcnt(8)
	v_mul_f32_e32 v2, 0x42800000, v36
	v_med3_f32 v4, v8, s72, v91
	v_med3_f32 v2, v2, s72, v91
	v_cvt_pk_fp8_f32 v75, v4, v2 op_sel:[0,0,1]
	v_mul_f32_e32 v2, 0x42800000, v5
	v_mul_f32_e32 v4, 0x42800000, v9
	v_med3_f32 v2, v2, s72, v91
	v_med3_f32 v8, v4, s72, v91
	v_mov_b32_e32 v4, 0
	v_cvt_pk_fp8_f32 v4, v2, v8
	v_mul_f32_e32 v5, 0x42800000, v17
	v_mul_f32_e32 v2, 0x42800000, v13
	v_med3_f32 v5, v5, s72, v91
	v_med3_f32 v2, v2, s72, v91
	v_cvt_pk_fp8_f32 v4, v5, v2 op_sel:[0,0,1]
	v_mul_f32_e32 v2, 0x42800000, v21
	v_mul_f32_e32 v5, 0x42800000, v25
	v_med3_f32 v2, v2, s72, v91
	v_med3_f32 v9, v5, s72, v91
	v_mov_b32_e32 v5, 0
	v_cvt_pk_fp8_f32 v5, v2, v9
	v_mul_f32_e32 v8, 0x42800000, v41
	v_mul_f32_e32 v2, 0x42800000, v37
	v_med3_f32 v8, v8, s72, v91
	v_med3_f32 v2, v2, s72, v91
	v_cvt_pk_fp8_f32 v5, v8, v2 op_sel:[0,0,1]
	v_mul_f32_e32 v2, 0x42800000, v6
	v_mul_f32_e32 v6, 0x42800000, v10
	v_med3_f32 v2, v2, s72, v91
	v_med3_f32 v6, v6, s72, v91
	v_mov_b32_e32 v8, 0
	v_cvt_pk_fp8_f32 v8, v2, v6
	v_mul_f32_e32 v9, 0x42800000, v18
	v_mul_f32_e32 v2, 0x42800000, v14
	v_med3_f32 v6, v9, s72, v91
	v_med3_f32 v2, v2, s72, v91
	v_cvt_pk_fp8_f32 v8, v6, v2 op_sel:[0,0,1]
	v_mul_f32_e32 v2, 0x42800000, v22
	v_mul_f32_e32 v6, 0x42800000, v26
	v_med3_f32 v2, v2, s72, v91
	v_med3_f32 v6, v6, s72, v91
	v_mov_b32_e32 v9, 0
	v_cvt_pk_fp8_f32 v9, v2, v6
	v_mul_f32_e32 v10, 0x42800000, v42
	v_mul_f32_e32 v2, 0x42800000, v38
	v_med3_f32 v6, v10, s72, v91
	v_med3_f32 v2, v2, s72, v91
	v_cvt_pk_fp8_f32 v9, v6, v2 op_sel:[0,0,1]
	v_mul_f32_e32 v2, 0x42800000, v7
	v_mul_f32_e32 v6, 0x42800000, v11
	v_med3_f32 v2, v2, s72, v91
	v_med3_f32 v10, v6, s72, v91
	v_mov_b32_e32 v6, 0
	v_cvt_pk_fp8_f32 v6, v2, v10
	v_mul_f32_e32 v7, 0x42800000, v19
	v_mul_f32_e32 v2, 0x42800000, v15
	v_med3_f32 v7, v7, s72, v91
	v_med3_f32 v2, v2, s72, v91
	v_cvt_pk_fp8_f32 v6, v7, v2 op_sel:[0,0,1]
	v_mul_f32_e32 v2, 0x42800000, v23
	v_mul_f32_e32 v7, 0x42800000, v27
	v_med3_f32 v2, v2, s72, v91
	v_med3_f32 v11, v7, s72, v91
	v_mov_b32_e32 v7, 0
	v_cvt_pk_fp8_f32 v7, v2, v11
	v_mul_f32_e32 v10, 0x42800000, v43
	v_mul_f32_e32 v2, 0x42800000, v39
	v_med3_f32 v10, v10, s72, v91
	v_med3_f32 v2, v2, s72, v91
	v_cvt_pk_fp8_f32 v7, v10, v2 op_sel:[0,0,1]
	v_add_u32_e32 v2, s33, v132
	ds_write2_b64 v2, v[74:75], v[4:5] offset1:9
	ds_write2_b64 v2, v[8:9], v[6:7] offset0:18 offset1:27
	v_add_u32_e32 v2, v131, v100
	s_waitcnt lgkmcnt(0)
	s_barrier
	ds_read2_b64 v[4:7], v2 offset1:1
	ds_read2_b64 v[8:11], v2 offset0:2 offset1:3
	s_add_u32 s0, s0, 0x40000
	s_addc_u32 s1, s1, 0
	s_add_i32 s45, s45, 1
	s_waitcnt lgkmcnt(1)
	global_store_dwordx4 v[72:73], v[4:7], off
	s_waitcnt lgkmcnt(0)
	global_store_dwordx4 v[72:73], v[8:11], off offset:16
	v_lshl_add_u64 v[72:73], v[72:73], 0, 64
	s_cmp_eq_u32 s0, 0x200000
	s_waitcnt vmcnt(2)
	v_mov_b32_e32 v4, v28
	v_mov_b32_e32 v5, v29
	v_mov_b32_e32 v6, v30
	v_mov_b32_e32 v7, v31
	v_mov_b32_e32 v8, v32
	v_mov_b32_e32 v9, v33
	v_mov_b32_e32 v10, v34
	v_mov_b32_e32 v11, v35
	v_mov_b32_e32 v16, v44
	v_mov_b32_e32 v17, v45
	v_mov_b32_e32 v18, v46
	v_mov_b32_e32 v19, v47
	v_mov_b32_e32 v12, v48
	v_mov_b32_e32 v13, v49
	v_mov_b32_e32 v14, v50
	v_mov_b32_e32 v15, v51
	v_mov_b32_e32 v20, v52
	v_mov_b32_e32 v21, v53
	v_mov_b32_e32 v22, v54
	v_mov_b32_e32 v23, v55
	v_mov_b32_e32 v24, v56
	v_mov_b32_e32 v25, v57
	v_mov_b32_e32 v26, v58
	v_mov_b32_e32 v27, v59
	v_mov_b32_e32 v40, v60
	v_mov_b32_e32 v41, v61
	v_mov_b32_e32 v42, v62
	v_mov_b32_e32 v43, v63
	v_mov_b32_e32 v36, v64
	v_mov_b32_e32 v37, v65
	v_mov_b32_e32 v38, v66
	v_mov_b32_e32 v39, v67
	s_barrier
	s_cbranch_scc1 .LBB0_115

; __device__ __forceinline__ f32x4 gld4_nt(const float* p) { return __builtin_nontemporal_load((const GAS f32x4*)p); }
; template <bool OUT8> __device__ __forceinline__ void conv_wide(const float* W0, const float* W1, int srcN, const float* ks0, const float* ks1, int kb_lo, int kb_hi, ...
;     ...
;     for (int kb = kb_lo; kb < kb_hi; ++kb) { const int k0 = kb * 64 + 8 * wid;
;         if (kb + 1 < kb_hi) {
; #pragma unroll
;             for (int j = 0; j < 8; ++j) vn[j] = gld4_nt(src + (size_t)(k0 + 64 + j) * srcN); }
;         if (ks0) {
; #pragma unroll
;             for (int j = 0; j < 8; ++j) { const int k = k0 + j; v[j] = v[j] * ((ks1 && k >= 512) ? ks1[k - 512] : ks0[k]); } }
;         if (shl) {
; #pragma unroll
;             for (int j = 0; j < 8; ++j) { b0 += v[j] * shl[k0 + j]; b1 += v[j] * shl[1024 + k0 + j]; } }
.LBB0_119:
	v_cndmask_b32_e64 v138, 0, 1, s[46:47]
	v_cmp_ne_u32_e64 s[0:1], 1, v138
	s_andn2_b64 vcc, exec, s[46:47]
	s_cbranch_vccnz .LBB0_121
	s_add_i32 s78, s76, s77
	s_add_i32 s79, s78, 0x16800
	s_add_i32 s80, s78, 0x17800
	v_mov_b32_e32 v138, s79
	v_mov_b32_e32 v142, s80
	ds_read_b128 v[138:141], v138
	ds_read_b128 v[142:145], v142
	s_add_i32 s79, s78, 0x16810
	s_add_i32 s78, s78, 0x17810
	s_waitcnt lgkmcnt(1)
	v_pk_fma_f32 v[44:45], v[48:49], v[138:139], v[44:45] op_sel_hi:[1,0,1]
	v_pk_fma_f32 v[42:43], v[46:47], v[138:139], v[42:43] op_sel_hi:[1,0,1]
	s_waitcnt lgkmcnt(0)
	v_pk_fma_f32 v[38:39], v[46:47], v[142:143], v[38:39] op_sel_hi:[1,0,1]
	v_pk_fma_f32 v[44:45], v[52:53], v[138:139], v[44:45] op_sel:[0,1,0]
	v_pk_fma_f32 v[42:43], v[50:51], v[138:139], v[42:43] op_sel:[0,1,0]
	v_pk_fma_f32 v[38:39], v[50:51], v[142:143], v[38:39] op_sel:[0,1,0]
	v_pk_fma_f32 v[40:41], v[48:49], v[142:143], v[40:41] op_sel_hi:[1,0,1]
	v_pk_fma_f32 v[44:45], v[60:61], v[140:141], v[44:45] op_sel_hi:[1,0,1]
	v_pk_fma_f32 v[42:43], v[58:59], v[140:141], v[42:43] op_sel_hi:[1,0,1]
	v_pk_fma_f32 v[146:147], v[58:59], v[144:145], v[38:39] op_sel_hi:[1,0,1]
	v_mov_b32_e32 v38, v141
	v_pk_fma_f32 v[40:41], v[52:53], v[142:143], v[40:41] op_sel:[0,1,0]
	v_pk_fma_f32 v[44:45], v[56:57], v[38:39], v[44:45] op_sel_hi:[1,0,1]
	v_pk_fma_f32 v[42:43], v[54:55], v[38:39], v[42:43] op_sel_hi:[1,0,1]
	v_mov_b32_e32 v38, s79
	v_pk_fma_f32 v[142:143], v[60:61], v[144:145], v[40:41] op_sel_hi:[1,0,1]
	ds_read_b128 v[38:41], v38
	v_mov_b32_e32 v138, s78
	ds_read_b128 v[138:141], v138
	v_mov_b32_e32 v144, v145
	v_pk_fma_f32 v[142:143], v[56:57], v[144:145], v[142:143] op_sel_hi:[1,0,1]
	v_pk_fma_f32 v[144:145], v[54:55], v[144:145], v[146:147] op_sel_hi:[1,0,1]
	s_waitcnt vmcnt(9) lgkmcnt(1)
	v_pk_fma_f32 v[44:45], v[64:65], v[38:39], v[44:45] op_sel_hi:[1,0,1]
	v_pk_fma_f32 v[42:43], v[62:63], v[38:39], v[42:43] op_sel_hi:[1,0,1]
	s_waitcnt lgkmcnt(0)
	v_pk_fma_f32 v[142:143], v[64:65], v[138:139], v[142:143] op_sel_hi:[1,0,1]
	v_pk_fma_f32 v[144:145], v[62:63], v[138:139], v[144:145] op_sel_hi:[1,0,1]
	s_waitcnt vmcnt(8)
	v_pk_fma_f32 v[44:45], v[72:73], v[38:39], v[44:45] op_sel:[0,1,0]
	v_pk_fma_f32 v[38:39], v[70:71], v[38:39], v[42:43] op_sel:[0,1,0]
	v_pk_fma_f32 v[42:43], v[72:73], v[138:139], v[142:143] op_sel:[0,1,0]
	v_pk_fma_f32 v[138:139], v[70:71], v[138:139], v[144:145] op_sel:[0,1,0]
	v_pk_fma_f32 v[44:45], v[68:69], v[40:41], v[44:45] op_sel_hi:[1,0,1]
	v_pk_fma_f32 v[38:39], v[66:67], v[40:41], v[38:39] op_sel_hi:[1,0,1]
	v_mov_b32_e32 v40, v41
	v_pk_fma_f32 v[142:143], v[68:69], v[140:141], v[42:43] op_sel_hi:[1,0,1]
	v_pk_fma_f32 v[138:139], v[66:67], v[140:141], v[138:139] op_sel_hi:[1,0,1]
	v_pk_fma_f32 v[42:43], v[74:75], v[40:41], v[38:39] op_sel_hi:[1,0,1]
	v_mov_b32_e32 v38, v141
	v_pk_fma_f32 v[44:45], v[76:77], v[40:41], v[44:45] op_sel_hi:[1,0,1]
	v_pk_fma_f32 v[40:41], v[76:77], v[38:39], v[142:143] op_sel_hi:[1,0,1]
	v_pk_fma_f32 v[38:39], v[74:75], v[38:39], v[138:139] op_sel_hi:[1,0,1]
; #define LAS __attribute__((address_space(3)))
; __device__ __forceinline__ unsigned cvt_pk_bf16(float lo, float hi) { unsigned r; asm volatile("v_cvt_pk_bf16_f32 %0, %1, %2" : "=v"(r) : "v"(lo), "v"(hi)); return r; }
; template <bool OUT8> __device__ __forceinline__ void conv_wide(const float* W0, const float* W1, int srcN, const float* ks0, const float* ks1, int kb_lo, int kb_hi, ...
;     ...
;         for (int c = 0; c < 4; ++c) { LAS unsigned char* tp = tile + (4 * lane + c) * RS;
;             if constexpr (OUT8) { u32x2 w; w.x = cvt4_fp8(v[0][c] * W8_SCALE, v[1][c] * W8_SCALE, v[2][c] * W8_SCALE, v[3][c] * W8_SCALE); w.y = cvt4_fp8(v[4][c] * W8_SCALE, v[5][c] * W8_SCALE, v[6][c] * W8_SCALE, v[7][c] * W8_SCALE);
;                 *(LAS u32x2*)(tp + 8 * wid) = w; }
;             else { u32x2 w0, w1; w0.x = cvt_pk_bf16(v[0][c], v[1][c]); w0.y = cvt_pk_bf16(v[2][c], v[3][c]); w1.x = cvt_pk_bf16(v[4][c], v[5][c]); w1.y = cvt_pk_bf16(v[6][c], v[7][c]);
;                 *(LAS u32x2*)(tp + 16 * wid) = w0; *(LAS u32x2*)(tp + 16 * wid + 8) = w1; } }
;         __syncthreads();
;         { const int row = tid >> 1, hf = tid & 1;
;           if constexpr (OUT8) { const LAS unsigned char* tp = tile + row * RS + hf * 32; unsigned char* dp = dst + (size_t)(n0 + row) * ldk + kb * 64 + hf * 32;
; #pragma unroll
;               for (int q = 0; q < 2; ++q) { const u32x2 lo = *(const LAS u32x2*)(tp + q * 16), hi2 = *(const LAS u32x2*)(tp + q * 16 + 8); gst16(dp + q * 16, (u32x4){lo.x, lo.y, hi2.x, hi2.y}); } }
;           else { const LAS unsigned char* tp = tile + row * RS + hf * 64; bf16_t* dp = (bf16_t*)dst + (size_t)(n0 + row) * ldk + kb * 64 + hf * 32;
; #pragma unroll
;               for (int q = 0; q < 4; ++q) { const u32x2 lo = *(const LAS u32x2*)(tp + q * 16), hi2 = *(const LAS u32x2*)(tp + q * 16 + 8); gst16(dp + q * 8, (u32x4){lo.x, lo.y, hi2.x, hi2.y}); } } }
;         __syncthreads();
; #pragma unroll
;         for (int j = 0; j < 8; ++j) v[j] = vn[j];
.LBB0_121:
	v_mul_f32_e32 v46, 0x42800000, v46
	v_mul_f32_e32 v50, 0x42800000, v50
	v_med3_f32 v46, v46, s72, v91
	v_med3_f32 v50, v50, s72, v91
	v_mov_b32_e32 v74, 0
	v_cvt_pk_fp8_f32 v74, v46, v50
	v_mul_f32_e32 v58, 0x42800000, v58
	v_mul_f32_e32 v46, 0x42800000, v54
	v_med3_f32 v50, v58, s72, v91
	v_med3_f32 v46, v46, s72, v91
	v_cvt_pk_fp8_f32 v74, v50, v46 op_sel:[0,0,1]
	s_waitcnt vmcnt(9)
	v_mul_f32_e32 v46, 0x42800000, v62
	s_waitcnt vmcnt(8)
	v_mul_f32_e32 v50, 0x42800000, v70
	v_med3_f32 v46, v46, s72, v91
	v_med3_f32 v50, v50, s72, v91
	v_mov_b32_e32 v75, 0
	v_cvt_pk_fp8_f32 v75, v46, v50
	v_mul_f32_e32 v54, 0x42800000, v66
	v_mul_f32_e32 v46, 0x42800000, v137
	v_med3_f32 v50, v54, s72, v91
	v_med3_f32 v46, v46, s72, v91
	v_cvt_pk_fp8_f32 v75, v50, v46 op_sel:[0,0,1]
	v_mul_f32_e32 v46, 0x42800000, v47
	v_mul_f32_e32 v47, 0x42800000, v51
	v_med3_f32 v51, v46, s72, v91
	v_med3_f32 v47, v47, s72, v91
	v_mov_b32_e32 v46, 0
	v_cvt_pk_fp8_f32 v46, v51, v47
	v_mul_f32_e32 v50, 0x42800000, v59
	v_mul_f32_e32 v47, 0x42800000, v55
	v_med3_f32 v50, v50, s72, v91
	v_med3_f32 v47, v47, s72, v91
	v_cvt_pk_fp8_f32 v46, v50, v47 op_sel:[0,0,1]
	v_mul_f32_e32 v47, 0x42800000, v63
	v_mul_f32_e32 v50, 0x42800000, v71
	v_med3_f32 v54, v47, s72, v91
	v_med3_f32 v50, v50, s72, v91
	v_mov_b32_e32 v47, 0
	v_cvt_pk_fp8_f32 v47, v54, v50
	v_mul_f32_e32 v51, 0x42800000, v67
	v_mul_f32_e32 v5, 0x42800000, v5
	v_med3_f32 v50, v51, s72, v91
	v_med3_f32 v5, v5, s72, v91
	v_cvt_pk_fp8_f32 v47, v50, v5 op_sel:[0,0,1]
	v_mul_f32_e32 v5, 0x42800000, v48
	v_mul_f32_e32 v48, 0x42800000, v52
	v_med3_f32 v5, v5, s72, v91
	v_med3_f32 v48, v48, s72, v91
	v_mov_b32_e32 v50, 0
	v_cvt_pk_fp8_f32 v50, v5, v48
	v_mul_f32_e32 v51, 0x42800000, v60
	v_mul_f32_e32 v5, 0x42800000, v56
	v_med3_f32 v48, v51, s72, v91
	v_med3_f32 v5, v5, s72, v91
	v_cvt_pk_fp8_f32 v50, v48, v5 op_sel:[0,0,1]
	v_mul_f32_e32 v5, 0x42800000, v64
	v_mul_f32_e32 v48, 0x42800000, v72
	v_med3_f32 v5, v5, s72, v91
	v_med3_f32 v48, v48, s72, v91
	v_mov_b32_e32 v51, 0
	v_cvt_pk_fp8_f32 v51, v5, v48
	v_mul_f32_e32 v52, 0x42800000, v68
	v_mul_f32_e32 v4, 0x42800000, v4
	v_med3_f32 v5, v52, s72, v91
	v_med3_f32 v4, v4, s72, v91
	v_cvt_pk_fp8_f32 v51, v5, v4 op_sel:[0,0,1]
	v_mul_f32_e32 v4, 0x42800000, v49
	v_mul_f32_e32 v5, 0x42800000, v53
	v_med3_f32 v4, v4, s72, v91
	v_med3_f32 v5, v5, s72, v91
	v_mov_b32_e32 v48, 0
	v_cvt_pk_fp8_f32 v48, v4, v5
	v_mul_f32_e32 v49, 0x42800000, v61
	v_mul_f32_e32 v4, 0x42800000, v57
	v_med3_f32 v5, v49, s72, v91
	v_med3_f32 v4, v4, s72, v91
	v_cvt_pk_fp8_f32 v48, v5, v4 op_sel:[0,0,1]
	v_mul_f32_e32 v4, 0x42800000, v65
	v_mul_f32_e32 v5, 0x42800000, v73
	v_med3_f32 v4, v4, s72, v91
	v_med3_f32 v5, v5, s72, v91
	v_mov_b32_e32 v49, 0
	v_cvt_pk_fp8_f32 v49, v4, v5
	v_mul_f32_e32 v52, 0x42800000, v69
	v_mul_f32_e32 v2, 0x42800000, v2
	v_med3_f32 v4, v52, s72, v91
	v_med3_f32 v2, v2, s72, v91
	v_cvt_pk_fp8_f32 v49, v4, v2 op_sel:[0,0,1]
	v_add_u32_e32 v4, s73, v132
	v_add_u32_e32 v2, v131, v100
	ds_write2_b64 v4, v[74:75], v[46:47] offset1:9
	ds_write2_b64 v4, v[50:51], v[48:49] offset0:18 offset1:27
	s_waitcnt lgkmcnt(0)
	s_barrier
	ds_read2_b64 v[46:49], v2 offset1:1
	ds_read2_b64 v[50:53], v2 offset0:2 offset1:3
	s_addk_i32 s77, 0x100
	s_add_i32 s78, s75, 1
	s_mov_b64 s[80:81], 0xe0000
	s_waitcnt lgkmcnt(1)
	global_store_dwordx4 v[128:129], v[46:49], off
	s_waitcnt lgkmcnt(0)
	global_store_dwordx4 v[128:129], v[50:53], off offset:16
	v_lshl_add_u64 v[128:129], v[128:129], 0, 64
	s_cmpk_eq_i32 s77, 0x700
	v_lshl_add_u64 v[126:127], v[126:127], 0, s[80:81]
	s_barrier
	s_waitcnt vmcnt(2)
	s_cbranch_scc0 .LBB0_117
	s_and_b64 vcc, exec, s[0:1]
	s_lshl_b32 s30, s75, 6
	s_cbranch_vccnz .LBB0_124
	s_lshl_b32 s46, s30, 2
	s_add_i32 s46, s74, s46
	s_lshl_b32 s47, s73, 2
	s_add_i32 s46, s46, s47
	v_mov_b32_e32 v5, s46
	ds_read_b128 v[46:49], v5 offset:24576
	ds_read_b128 v[50:53], v5 offset:28672
	ds_read_b128 v[54:57], v5 offset:24592
	ds_read_b128 v[58:61], v5 offset:28688
	s_waitcnt lgkmcnt(3)
	v_pk_fma_f32 v[42:43], v[6:7], v[46:47], v[42:43] op_sel_hi:[1,0,1]
	v_pk_fma_f32 v[44:45], v[8:9], v[46:47], v[44:45] op_sel_hi:[1,0,1]
	s_waitcnt lgkmcnt(2)
	v_pk_fma_f32 v[38:39], v[6:7], v[50:51], v[38:39] op_sel_hi:[1,0,1]
	v_pk_fma_f32 v[40:41], v[8:9], v[50:51], v[40:41] op_sel_hi:[1,0,1]
	v_pk_fma_f32 v[44:45], v[12:13], v[46:47], v[44:45] op_sel:[0,1,0]
	v_pk_fma_f32 v[42:43], v[10:11], v[46:47], v[42:43] op_sel:[0,1,0]
	v_pk_fma_f32 v[40:41], v[12:13], v[50:51], v[40:41] op_sel:[0,1,0]
	v_pk_fma_f32 v[38:39], v[10:11], v[50:51], v[38:39] op_sel:[0,1,0]
	v_pk_fma_f32 v[42:43], v[18:19], v[48:49], v[42:43] op_sel_hi:[1,0,1]
	v_pk_fma_f32 v[44:45], v[20:21], v[48:49], v[44:45] op_sel_hi:[1,0,1]
	v_mov_b32_e32 v46, v49
	v_pk_fma_f32 v[38:39], v[18:19], v[52:53], v[38:39] op_sel_hi:[1,0,1]
	v_pk_fma_f32 v[40:41], v[20:21], v[52:53], v[40:41] op_sel_hi:[1,0,1]
	v_pk_fma_f32 v[44:45], v[16:17], v[46:47], v[44:45] op_sel_hi:[1,0,1]
	v_pk_fma_f32 v[42:43], v[14:15], v[46:47], v[42:43] op_sel_hi:[1,0,1]
	v_mov_b32_e32 v46, v53
	v_pk_fma_f32 v[40:41], v[16:17], v[46:47], v[40:41] op_sel_hi:[1,0,1]
	v_pk_fma_f32 v[38:39], v[14:15], v[46:47], v[38:39] op_sel_hi:[1,0,1]
	s_waitcnt lgkmcnt(1)
	v_pk_fma_f32 v[42:43], v[22:23], v[54:55], v[42:43] op_sel_hi:[1,0,1]
	v_pk_fma_f32 v[44:45], v[24:25], v[54:55], v[44:45] op_sel_hi:[1,0,1]
	s_waitcnt lgkmcnt(0)
	v_pk_fma_f32 v[38:39], v[22:23], v[58:59], v[38:39] op_sel_hi:[1,0,1]
	v_pk_fma_f32 v[40:41], v[24:25], v[58:59], v[40:41] op_sel_hi:[1,0,1]
	v_pk_fma_f32 v[44:45], v[28:29], v[54:55], v[44:45] op_sel:[0,1,0]
	v_pk_fma_f32 v[42:43], v[26:27], v[54:55], v[42:43] op_sel:[0,1,0]
	v_pk_fma_f32 v[40:41], v[28:29], v[58:59], v[40:41] op_sel:[0,1,0]
	v_pk_fma_f32 v[38:39], v[26:27], v[58:59], v[38:39] op_sel:[0,1,0]
	v_pk_fma_f32 v[42:43], v[34:35], v[56:57], v[42:43] op_sel_hi:[1,0,1]
	v_pk_fma_f32 v[44:45], v[36:37], v[56:57], v[44:45] op_sel_hi:[1,0,1]
	v_mov_b32_e32 v46, v57
	v_pk_fma_f32 v[38:39], v[34:35], v[60:61], v[38:39] op_sel_hi:[1,0,1]
	v_pk_fma_f32 v[40:41], v[36:37], v[60:61], v[40:41] op_sel_hi:[1,0,1]
	v_pk_fma_f32 v[44:45], v[32:33], v[46:47], v[44:45] op_sel_hi:[1,0,1]
	v_pk_fma_f32 v[42:43], v[30:31], v[46:47], v[42:43] op_sel_hi:[1,0,1]
	v_mov_b32_e32 v46, v61
	v_pk_fma_f32 v[40:41], v[32:33], v[46:47], v[40:41] op_sel_hi:[1,0,1]
	v_pk_fma_f32 v[38:39], v[30:31], v[46:47], v[38:39] op_sel_hi:[1,0,1]
